# v068 + barrier leader issues the XGEN release atomic before its own acquire-side buffer_inv (members invalidate themselves after observing XGEN)
# baseline (speedup 1.0000x reference)
; __device__ __forceinline__ unsigned xb_add(unsigned* p, unsigned v) { return __hip_atomic_fetch_add(p, v, __ATOMIC_RELAXED, __HIP_MEMORY_SCOPE_AGENT); }
; __device__ __forceinline__ void xcd_barrier(const XcdBarrier& b, const int tid) {
;     ...
;             __builtin_amdgcn_fence(__ATOMIC_ACQUIRE, "agent");
;             xb_add(&bar[XB_XGEN(b.x)], 1u);
;             asm volatile("s_waitcnt vmcnt(0)" ::: "memory");
.LBB0_761:
	s_or_b64 exec, exec, s[40:41]
	s_mov_b64 s[40:41], exec
	v_mbcnt_lo_u32_b32 v0, s40, 0
	v_mbcnt_hi_u32_b32 v0, s41, v0
	v_cmp_eq_u32_e32 vcc, 0, v0
	s_waitcnt vmcnt(0)
	s_and_saveexec_b64 s[42:43], vcc
	s_cbranch_execz .LBB0_763
	s_bcnt1_i32_b64 s7, s[40:41]
	v_readlane_b32 s22, v252, 11
	v_mov_b32_e32 v0, s7
	v_readlane_b32 s23, v252, 12
	s_nop 4
	global_atomic_add v1, v0, s[22:23]
.LBB0_763:
	s_or_b64 exec, exec, s[42:43]
	buffer_inv sc1
	s_waitcnt vmcnt(0)

; __device__ __forceinline__ unsigned xb_add(unsigned* p, unsigned v) { return __hip_atomic_fetch_add(p, v, __ATOMIC_RELAXED, __HIP_MEMORY_SCOPE_AGENT); }
; __device__ __forceinline__ void xcd_barrier(const XcdBarrier& b, const int tid) {
;     ...
;             __builtin_amdgcn_fence(__ATOMIC_ACQUIRE, "agent");
;             xb_add(&bar[XB_XGEN(b.x)], 1u);
;             asm volatile("s_waitcnt vmcnt(0)" ::: "memory");
.LBB0_1833:
	s_or_b64 exec, exec, s[40:41]
	s_mov_b64 s[40:41], exec
	v_mbcnt_lo_u32_b32 v0, s40, 0
	v_mbcnt_hi_u32_b32 v0, s41, v0
	v_cmp_eq_u32_e32 vcc, 0, v0
	s_waitcnt vmcnt(0)
	s_and_saveexec_b64 s[42:43], vcc
	s_cbranch_execz .LBB0_1835
	s_bcnt1_i32_b64 s6, s[40:41]
	v_mov_b32_e32 v0, s6
	v_readlane_b32 s6, v252, 11
	v_readlane_b32 s7, v252, 12
	s_nop 4
	global_atomic_add v1, v0, s[6:7]
